# v010 + prologue: converted-weight stores use the default write-back policy instead of nt (Infinity Cache may absorb part of the write traffic)
# baseline (speedup 1.0000x reference)
; #define LAS __attribute__((address_space(3)))
; __device__ __forceinline__ unsigned pk2(float lo, float hi) { f32x2 v = {lo, hi}; return __builtin_bit_cast(unsigned, __builtin_convertvector(v, bf2_t)); }
;     const float* s = src + (size_t)k0 * ld + c0;
;     const int kr = lane >> 4, nq = lane & 15;
; #pragma unroll 4
;     for (int i = 0; i < 16; ++i) { const int k = 4 * i + kr; const f32x4 v = __builtin_nontemporal_load((const f32x4*)(s + (size_t)k * ld + 4 * nq));
;         LAS float* d = scr + k * 65 + 4 * nq; d[0] = v[0]; d[1] = v[1]; d[2] = v[2]; d[3] = v[3]; }
;     asm volatile("s_waitcnt lgkmcnt(0)" ::: "memory");
;     const int c = lane & 7;
; #pragma unroll
;     for (int j = 0; j < 8; ++j) { const int n = (lane >> 3) + 8 * j; const int sc_ = qkperm ? ((n & 1) * 32 + (n >> 1)) : n; const LAS float* p = scr + (8 * c) * 65 + sc_;
;         u32x4 o; o.x = pk2(p[0] * scale, p[65] * scale); o.y = pk2(p[130] * scale, p[195] * scale); o.z = pk2(p[260] * scale, p[325] * scale); o.w = pk2(p[390] * scale, p[455] * scale);
;         __builtin_nontemporal_store(o, (u32x4*)(dst + (size_t)(n0 + n) * Kd + k0 + 8 * c)); }
;     asm volatile("s_waitcnt lgkmcnt(0)" ::: "memory");
; }
; __device__ __forceinline__ void conv_item(Frame& F, const Args& a, int it, LAS float* scr, int lane) {
;     ...
;         { const int ie = r / (56 * 16), q = r % (56 * 16), kt = q / 16, nt = q % 16, i = ie >> 3, e = ie & 7;
;             tr_item((a.in[26] + F.zo) + (size_t)ie * DFE * D, D, 64 * kt, 64 * nt, (bf16*)(ws + WS_EXP + i * EXP_STRIDE) + (size_t)NE * 2 * DFE * D + (size_t)e * D * DFE, DFE, 64 * nt, false, scr, lane); }
.LBB13_48:
	v_lshl_add_u64 v[52:53], v[20:21], 0, s[18:19]
	v_add_co_u32_e32 v44, vcc, 0x4000, v52
	global_load_dwordx4 v[40:43], v[52:53], off nt
	s_nop 0
	v_addc_co_u32_e32 v45, vcc, 0, v53, vcc
	v_add_co_u32_e32 v48, vcc, 0x8000, v52
	global_load_dwordx4 v[44:47], v[44:45], off nt
	s_nop 0
	v_addc_co_u32_e32 v49, vcc, 0, v53, vcc
	v_add_co_u32_e32 v52, vcc, 0xc000, v52
	global_load_dwordx4 v[48:51], v[48:49], off nt
	s_nop 0
	v_addc_co_u32_e32 v53, vcc, 0, v53, vcc
	global_load_dwordx4 v[52:55], v[52:53], off nt
	s_add_u32 s18, s18, 0x10000
	s_addc_u32 s19, s19, 0
	v_add_u32_e32 v39, 0x410, v4
	v_add_u32_e32 v56, 0x418, v4
	v_add_u32_e32 v57, 0x820, v4
	v_add_u32_e32 v58, 0x828, v4
	v_add_u32_e32 v59, 0xc30, v4
	v_add_u32_e32 v60, 0xc38, v4
	s_cmp_lg_u32 s18, 0x40000
	s_waitcnt vmcnt(3)
	ds_write2_b32 v4, v40, v41 offset1:1
	ds_write2_b32 v4, v42, v43 offset0:2 offset1:3
	v_add_u32_e32 v4, 0x1040, v4
	s_waitcnt vmcnt(2)
	ds_write2_b32 v39, v44, v45 offset1:1
	ds_write2_b32 v56, v46, v47 offset1:1
	s_waitcnt vmcnt(1)
	ds_write2_b32 v57, v48, v49 offset1:1
	ds_write2_b32 v58, v50, v51 offset1:1
	s_waitcnt vmcnt(0)
	ds_write2_b32 v59, v52, v53 offset1:1
	ds_write2_b32 v60, v54, v55 offset1:1
	s_cbranch_scc1 .LBB13_48
	s_and_b32 s18, 0xffff, s28
	s_lshr_b32 s19, s18, 3
	s_lshl_b32 s28, s29, 6
	s_lshl_b32 s18, s18, 10
	s_and_b32 s28, s28, 0x3c0
	s_mul_i32 s19, s19, 0xa800000
	s_and_b32 s18, s18, 0x1c00
	s_add_u32 s19, s33, s19
	s_addc_u32 s29, s43, 0
	s_mulk_i32 s18, 0x1c00
	s_add_u32 s18, s19, s18
	s_waitcnt lgkmcnt(0)
	v_add_u32_e32 v39, 0x400, v22
	s_addc_u32 s19, s29, 0
	s_lshl_b32 s6, s6, 1
	ds_read2_b32 v[44:45], v22 offset0:65 offset1:73
	ds_read2_b32 v[46:47], v22 offset1:8
	ds_read2_b32 v[48:49], v22 offset0:130 offset1:138
	ds_read2_b32 v[50:51], v22 offset0:195 offset1:203
	ds_read2_b32 v[52:53], v39 offset0:4 offset1:12
	ds_read2_b32 v[54:55], v39 offset0:69 offset1:77
	ds_read2_b32 v[56:57], v39 offset0:134 offset1:142
	ds_read2_b32 v[58:59], v39 offset0:199 offset1:207
	s_add_u32 s18, s18, s6
	s_addc_u32 s19, s19, 0
	v_lshlrev_b32_e32 v4, 1, v2
	v_lshl_add_u64 v[20:21], s[18:19], 0, v[4:5]
	v_or_b32_e32 v4, s28, v1
	v_lshl_add_u64 v[20:21], v[20:21], 0, s[8:9]
	v_mul_u32_u24_e32 v4, 0x1c00, v4
	s_waitcnt lgkmcnt(6)
	v_cvt_pk_bf16_f32 v40, v46, v44
	s_waitcnt lgkmcnt(4)
	v_cvt_pk_bf16_f32 v41, v48, v50
	s_waitcnt lgkmcnt(2)
	v_cvt_pk_bf16_f32 v42, v52, v54
	s_waitcnt lgkmcnt(0)
	v_cvt_pk_bf16_f32 v43, v56, v58
	v_lshl_add_u64 v[60:61], v[20:21], 0, v[4:5]
	global_store_dwordx4 v[60:61], v[40:43], off
	v_or_b32_e32 v4, s28, v23
	v_mul_u32_u24_e32 v4, 0x1c00, v4
	v_cvt_pk_bf16_f32 v40, v47, v45
	v_cvt_pk_bf16_f32 v41, v49, v51
	v_cvt_pk_bf16_f32 v42, v53, v55
	v_cvt_pk_bf16_f32 v43, v57, v59
	ds_read2_b32 v[46:47], v22 offset0:16 offset1:24
	ds_read2_b32 v[48:49], v22 offset0:81 offset1:89
	ds_read2_b32 v[50:51], v22 offset0:146 offset1:154
	ds_read2_b32 v[52:53], v22 offset0:211 offset1:219
	ds_read2_b32 v[54:55], v39 offset0:20 offset1:28
	ds_read2_b32 v[56:57], v39 offset0:85 offset1:93
	ds_read2_b32 v[58:59], v39 offset0:150 offset1:158
	ds_read2_b32 v[60:61], v39 offset0:215 offset1:223
	v_lshl_add_u64 v[44:45], v[20:21], 0, v[4:5]
	v_or_b32_e32 v4, s28, v24
	v_mul_u32_u24_e32 v4, 0x1c00, v4
	global_store_dwordx4 v[44:45], v[40:43], off
	v_lshl_add_u64 v[44:45], v[20:21], 0, v[4:5]
	v_or_b32_e32 v4, s28, v25
	s_waitcnt lgkmcnt(6)
	v_cvt_pk_bf16_f32 v40, v46, v48
	s_waitcnt lgkmcnt(4)
	v_cvt_pk_bf16_f32 v41, v50, v52
	s_waitcnt lgkmcnt(2)
	v_cvt_pk_bf16_f32 v42, v54, v56
	s_waitcnt lgkmcnt(0)
	v_cvt_pk_bf16_f32 v43, v58, v60
	global_store_dwordx4 v[44:45], v[40:43], off
	v_mul_u32_u24_e32 v4, 0x1c00, v4
	v_lshl_add_u64 v[44:45], v[20:21], 0, v[4:5]
	v_cvt_pk_bf16_f32 v40, v47, v49
	v_cvt_pk_bf16_f32 v41, v51, v53
	v_cvt_pk_bf16_f32 v42, v55, v57
	v_cvt_pk_bf16_f32 v43, v59, v61
	ds_read2_b32 v[46:47], v22 offset0:32 offset1:40
	ds_read2_b32 v[48:49], v22 offset0:97 offset1:105
	ds_read2_b32 v[50:51], v22 offset0:162 offset1:170
	ds_read2_b32 v[52:53], v22 offset0:227 offset1:235
	ds_read2_b32 v[54:55], v39 offset0:36 offset1:44
	ds_read2_b32 v[56:57], v39 offset0:101 offset1:109
	ds_read2_b32 v[58:59], v39 offset0:166 offset1:174
	ds_read2_b32 v[60:61], v39 offset0:231 offset1:239
	v_or_b32_e32 v4, s28, v26
	v_mul_u32_u24_e32 v4, 0x1c00, v4
	global_store_dwordx4 v[44:45], v[40:43], off
	v_lshl_add_u64 v[44:45], v[20:21], 0, v[4:5]
	v_or_b32_e32 v4, s28, v27
	s_waitcnt lgkmcnt(6)
	v_cvt_pk_bf16_f32 v40, v46, v48
	s_waitcnt lgkmcnt(4)
	v_cvt_pk_bf16_f32 v41, v50, v52
	s_waitcnt lgkmcnt(2)
	v_cvt_pk_bf16_f32 v42, v54, v56
	s_waitcnt lgkmcnt(0)
	v_cvt_pk_bf16_f32 v43, v58, v60
	global_store_dwordx4 v[44:45], v[40:43], off
	v_mul_u32_u24_e32 v4, 0x1c00, v4
	v_lshl_add_u64 v[44:45], v[20:21], 0, v[4:5]
	v_cvt_pk_bf16_f32 v40, v47, v49
	v_cvt_pk_bf16_f32 v41, v51, v53
	v_cvt_pk_bf16_f32 v42, v55, v57
	v_cvt_pk_bf16_f32 v43, v59, v61
	ds_read2_b32 v[46:47], v22 offset0:48 offset1:56
	ds_read2_b32 v[48:49], v22 offset0:113 offset1:121
	ds_read2_b32 v[50:51], v22 offset0:178 offset1:186
	ds_read2_b32 v[52:53], v22 offset0:243 offset1:251
	ds_read2_b32 v[54:55], v39 offset0:52 offset1:60
	ds_read2_b32 v[56:57], v39 offset0:117 offset1:125
	ds_read2_b32 v[58:59], v39 offset0:182 offset1:190
	ds_read2_b32 v[60:61], v39 offset0:247 offset1:255
	v_or_b32_e32 v4, s28, v28
	v_mul_u32_u24_e32 v4, 0x1c00, v4
	global_store_dwordx4 v[44:45], v[40:43], off
	v_lshl_add_u64 v[44:45], v[20:21], 0, v[4:5]
	v_or_b32_e32 v4, s28, v29
	s_waitcnt lgkmcnt(6)
	v_cvt_pk_bf16_f32 v40, v46, v48
	s_waitcnt lgkmcnt(4)
	v_cvt_pk_bf16_f32 v41, v50, v52
	s_waitcnt lgkmcnt(2)
	v_cvt_pk_bf16_f32 v42, v54, v56
	s_waitcnt lgkmcnt(0)
	v_cvt_pk_bf16_f32 v43, v58, v60
	v_mul_u32_u24_e32 v4, 0x1c00, v4
	global_store_dwordx4 v[44:45], v[40:43], off
	v_lshl_add_u64 v[20:21], v[20:21], 0, v[4:5]
	s_mov_b64 s[18:19], 0
	v_cvt_pk_bf16_f32 v40, v47, v49
	v_cvt_pk_bf16_f32 v41, v51, v53
	v_cvt_pk_bf16_f32 v42, v55, v57
	v_cvt_pk_bf16_f32 v43, v59, v61
	global_store_dwordx4 v[20:21], v[40:43], off
	s_waitcnt lgkmcnt(0)

; #define LAS __attribute__((address_space(3)))
; __device__ __forceinline__ unsigned pk2(float lo, float hi) { f32x2 v = {lo, hi}; return __builtin_bit_cast(unsigned, __builtin_convertvector(v, bf2_t)); }
;     const float* s = src + (size_t)k0 * ld + c0;
;     const int kr = lane >> 4, nq = lane & 15;
; #pragma unroll 4
;     for (int i = 0; i < 16; ++i) { const int k = 4 * i + kr; const f32x4 v = __builtin_nontemporal_load((const f32x4*)(s + (size_t)k * ld + 4 * nq));
;         LAS float* d = scr + k * 65 + 4 * nq; d[0] = v[0]; d[1] = v[1]; d[2] = v[2]; d[3] = v[3]; }
;     asm volatile("s_waitcnt lgkmcnt(0)" ::: "memory");
;     const int c = lane & 7;
; #pragma unroll
;     for (int j = 0; j < 8; ++j) { const int n = (lane >> 3) + 8 * j; const int sc_ = qkperm ? ((n & 1) * 32 + (n >> 1)) : n; const LAS float* p = scr + (8 * c) * 65 + sc_;
;         u32x4 o; o.x = pk2(p[0] * scale, p[65] * scale); o.y = pk2(p[130] * scale, p[195] * scale); o.z = pk2(p[260] * scale, p[325] * scale); o.w = pk2(p[390] * scale, p[455] * scale);
;         __builtin_nontemporal_store(o, (u32x4*)(dst + (size_t)(n0 + n) * Kd + k0 + 8 * c)); }
;     asm volatile("s_waitcnt lgkmcnt(0)" ::: "memory");
; }
; __device__ __forceinline__ void conv_item(Frame& F, const Args& a, int it, LAS float* scr, int lane) {
;     ...
;         if (r < TI_EGU) { const int ie = r / (16 * 112), q = r % (16 * 112), kt = q / 112, nt = q % 112, i = ie >> 3, e = ie & 7;
;             const int pn = nt >> 2, bj = (nt >> 1) & 1, hf = nt & 1;
;             const float* src = (bj ? (a.in[25] + F.zo) : (a.in[24] + F.zo)) + (size_t)ie * D * DFE;
;             tr_item(src, DFE, 64 * kt, 128 * pn + 64 * hf, (bf16*)(ws + WS_EXP + i * EXP_STRIDE) + (size_t)e * 2 * DFE * D, D, 64 * nt, false, scr, lane); break; }
.LBB13_52:
	v_lshl_add_u64 v[52:53], v[20:21], 0, s[18:19]
	v_add_co_u32_e32 v44, vcc, 0xe000, v52
	global_load_dwordx4 v[40:43], v[52:53], off nt
	s_nop 0
	v_addc_co_u32_e32 v45, vcc, 0, v53, vcc
	v_add_co_u32_e32 v48, vcc, 0x1c000, v52
	global_load_dwordx4 v[44:47], v[44:45], off nt
	s_nop 0
	v_addc_co_u32_e32 v49, vcc, 0, v53, vcc
	v_add_co_u32_e32 v52, vcc, 0x2a000, v52
	global_load_dwordx4 v[48:51], v[48:49], off nt
	s_nop 0
	v_addc_co_u32_e32 v53, vcc, 0, v53, vcc
	global_load_dwordx4 v[52:55], v[52:53], off nt
	s_add_u32 s18, s18, 0x38000
	s_addc_u32 s19, s19, 0
	v_add_u32_e32 v39, 0x410, v4
	v_add_u32_e32 v56, 0x418, v4
	v_add_u32_e32 v57, 0x820, v4
	v_add_u32_e32 v58, 0x828, v4
	v_add_u32_e32 v59, 0xc30, v4
	v_add_u32_e32 v60, 0xc38, v4
	s_cmp_lg_u32 s18, 0xe0000
	s_waitcnt vmcnt(3)
	ds_write2_b32 v4, v40, v41 offset1:1
	ds_write2_b32 v4, v42, v43 offset0:2 offset1:3
	v_add_u32_e32 v4, 0x1040, v4
	s_waitcnt vmcnt(2)
	ds_write2_b32 v39, v44, v45 offset1:1
	ds_write2_b32 v56, v46, v47 offset1:1
	s_waitcnt vmcnt(1)
	ds_write2_b32 v57, v48, v49 offset1:1
	ds_write2_b32 v58, v50, v51 offset1:1
	s_waitcnt vmcnt(0)
	ds_write2_b32 v59, v52, v53 offset1:1
	ds_write2_b32 v60, v54, v55 offset1:1
	s_cbranch_scc1 .LBB13_52
	s_lshl_b32 s18, s28, 1
	s_lshr_b32 s19, s28, 3
	s_and_b32 s18, s18, 14
	s_mul_i32 s19, s19, 0xa800000
	s_add_u32 s19, s5, s19
	s_addc_u32 s28, s15, 0
	s_mul_i32 s18, s18, 0x700000
	s_add_u32 s18, s19, s18
	s_waitcnt lgkmcnt(0)
	v_add_u32_e32 v39, 0x400, v22
	s_addc_u32 s19, s28, 0
	s_lshl_b32 s28, s29, 1
	ds_read2_b32 v[20:21], v22 offset0:65 offset1:73
	ds_read2_b32 v[44:45], v22 offset1:8
	ds_read2_b32 v[46:47], v22 offset0:130 offset1:138
	ds_read2_b32 v[48:49], v22 offset0:195 offset1:203
	ds_read2_b32 v[50:51], v39 offset0:4 offset1:12
	ds_read2_b32 v[52:53], v39 offset0:69 offset1:77
	ds_read2_b32 v[54:55], v39 offset0:134 offset1:142
	ds_read2_b32 v[56:57], v39 offset0:199 offset1:207
	s_add_u32 s18, s18, s28
	s_addc_u32 s19, s19, 0
	v_lshlrev_b32_e32 v4, 1, v2
	v_lshl_add_u64 v[58:59], s[18:19], 0, v[4:5]
	v_or_b32_e32 v4, s6, v1
	v_lshlrev_b32_e32 v4, 11, v4
	s_waitcnt lgkmcnt(6)
	v_cvt_pk_bf16_f32 v40, v44, v20
	s_waitcnt lgkmcnt(4)
	v_cvt_pk_bf16_f32 v41, v46, v48
	s_waitcnt lgkmcnt(2)
	v_cvt_pk_bf16_f32 v42, v50, v52
	s_waitcnt lgkmcnt(0)
	v_cvt_pk_bf16_f32 v43, v54, v56
	v_lshl_add_u64 v[60:61], v[58:59], 0, v[4:5]
	global_store_dwordx4 v[60:61], v[40:43], off
	v_or_b32_e32 v4, s6, v23
	v_lshlrev_b32_e32 v4, 11, v4
	v_cvt_pk_bf16_f32 v40, v45, v21
	v_cvt_pk_bf16_f32 v41, v47, v49
	v_cvt_pk_bf16_f32 v42, v51, v53
	v_cvt_pk_bf16_f32 v43, v55, v57
	ds_read2_b32 v[44:45], v22 offset0:81 offset1:89
	ds_read2_b32 v[46:47], v22 offset0:16 offset1:24
	ds_read2_b32 v[48:49], v22 offset0:146 offset1:154
	ds_read2_b32 v[50:51], v22 offset0:211 offset1:219
	ds_read2_b32 v[52:53], v39 offset0:20 offset1:28
	ds_read2_b32 v[54:55], v39 offset0:85 offset1:93
	ds_read2_b32 v[56:57], v39 offset0:150 offset1:158
	ds_read2_b32 v[60:61], v39 offset0:215 offset1:223
	v_lshl_add_u64 v[20:21], v[58:59], 0, v[4:5]
	v_or_b32_e32 v4, s6, v24
	v_lshlrev_b32_e32 v4, 11, v4
	global_store_dwordx4 v[20:21], v[40:43], off
	v_lshl_add_u64 v[20:21], v[58:59], 0, v[4:5]
	v_or_b32_e32 v4, s6, v25
	s_waitcnt lgkmcnt(6)
	v_cvt_pk_bf16_f32 v40, v46, v44
	s_waitcnt lgkmcnt(4)
	v_cvt_pk_bf16_f32 v41, v48, v50
	s_waitcnt lgkmcnt(2)
	v_cvt_pk_bf16_f32 v42, v52, v54
	s_waitcnt lgkmcnt(0)
	v_cvt_pk_bf16_f32 v43, v56, v60
	global_store_dwordx4 v[20:21], v[40:43], off
	v_lshlrev_b32_e32 v4, 11, v4
	v_lshl_add_u64 v[20:21], v[58:59], 0, v[4:5]
	v_cvt_pk_bf16_f32 v40, v47, v45
	v_cvt_pk_bf16_f32 v41, v49, v51
	v_cvt_pk_bf16_f32 v42, v53, v55
	v_cvt_pk_bf16_f32 v43, v57, v61
	ds_read2_b32 v[44:45], v22 offset0:32 offset1:40
	ds_read2_b32 v[46:47], v22 offset0:97 offset1:105
	ds_read2_b32 v[48:49], v22 offset0:162 offset1:170
	ds_read2_b32 v[50:51], v22 offset0:227 offset1:235
	ds_read2_b32 v[52:53], v39 offset0:36 offset1:44
	ds_read2_b32 v[54:55], v39 offset0:101 offset1:109
	ds_read2_b32 v[56:57], v39 offset0:166 offset1:174
	ds_read2_b32 v[60:61], v39 offset0:231 offset1:239
	v_or_b32_e32 v4, s6, v26
	v_lshlrev_b32_e32 v4, 11, v4
	global_store_dwordx4 v[20:21], v[40:43], off
	v_lshl_add_u64 v[20:21], v[58:59], 0, v[4:5]
	v_or_b32_e32 v4, s6, v27
	s_waitcnt lgkmcnt(6)
	v_cvt_pk_bf16_f32 v40, v44, v46
	s_waitcnt lgkmcnt(4)
	v_cvt_pk_bf16_f32 v41, v48, v50
	s_waitcnt lgkmcnt(2)
	v_cvt_pk_bf16_f32 v42, v52, v54
	s_waitcnt lgkmcnt(0)
	v_cvt_pk_bf16_f32 v43, v56, v60
	global_store_dwordx4 v[20:21], v[40:43], off
	v_lshlrev_b32_e32 v4, 11, v4
	v_lshl_add_u64 v[20:21], v[58:59], 0, v[4:5]
	v_cvt_pk_bf16_f32 v40, v45, v47
	v_cvt_pk_bf16_f32 v41, v49, v51
	v_cvt_pk_bf16_f32 v42, v53, v55
	v_cvt_pk_bf16_f32 v43, v57, v61
	ds_read2_b32 v[44:45], v22 offset0:48 offset1:56
	ds_read2_b32 v[46:47], v22 offset0:113 offset1:121
	ds_read2_b32 v[48:49], v22 offset0:178 offset1:186
	ds_read2_b32 v[50:51], v22 offset0:243 offset1:251
	ds_read2_b32 v[52:53], v39 offset0:52 offset1:60
	ds_read2_b32 v[54:55], v39 offset0:117 offset1:125
	ds_read2_b32 v[56:57], v39 offset0:182 offset1:190
	ds_read2_b32 v[60:61], v39 offset0:247 offset1:255
	v_or_b32_e32 v4, s6, v28
	v_lshlrev_b32_e32 v4, 11, v4
	global_store_dwordx4 v[20:21], v[40:43], off
	v_lshl_add_u64 v[20:21], v[58:59], 0, v[4:5]
	v_or_b32_e32 v4, s6, v29
	s_waitcnt lgkmcnt(6)
	v_cvt_pk_bf16_f32 v40, v44, v46
	s_waitcnt lgkmcnt(4)
	v_cvt_pk_bf16_f32 v41, v48, v50
	s_waitcnt lgkmcnt(2)
	v_cvt_pk_bf16_f32 v42, v52, v54
	s_waitcnt lgkmcnt(0)
	v_cvt_pk_bf16_f32 v43, v56, v60
	v_lshlrev_b32_e32 v4, 11, v4
	global_store_dwordx4 v[20:21], v[40:43], off
	v_lshl_add_u64 v[20:21], v[58:59], 0, v[4:5]
	s_nop 0
	v_cvt_pk_bf16_f32 v40, v45, v47
	v_cvt_pk_bf16_f32 v41, v49, v51
	v_cvt_pk_bf16_f32 v42, v53, v55
	v_cvt_pk_bf16_f32 v43, v57, v61
	global_store_dwordx4 v[20:21], v[40:43], off
	s_waitcnt lgkmcnt(0)

; #define LAS __attribute__((address_space(3)))
; __device__ __forceinline__ unsigned pk2(float lo, float hi) { f32x2 v = {lo, hi}; return __builtin_bit_cast(unsigned, __builtin_convertvector(v, bf2_t)); }
;     ...
;     for (int i = 0; i < 16; ++i) { const int k = 4 * i + kr; const f32x4 v = __builtin_nontemporal_load((const f32x4*)(s + (size_t)k * ld + 4 * nq));
;         LAS float* d = scr + k * 65 + 4 * nq; d[0] = v[0]; d[1] = v[1]; d[2] = v[2]; d[3] = v[3]; }
;     asm volatile("s_waitcnt lgkmcnt(0)" ::: "memory");
;     const int c = lane & 7;
; #pragma unroll
;     for (int j = 0; j < 8; ++j) { const int n = (lane >> 3) + 8 * j; const int sc_ = qkperm ? ((n & 1) * 32 + (n >> 1)) : n; const LAS float* p = scr + (8 * c) * 65 + sc_;
;         u32x4 o; o.x = pk2(p[0] * scale, p[65] * scale); o.y = pk2(p[130] * scale, p[195] * scale); o.z = pk2(p[260] * scale, p[325] * scale); o.w = pk2(p[390] * scale, p[455] * scale);
;         __builtin_nontemporal_store(o, (u32x4*)(dst + (size_t)(n0 + n) * Kd + k0 + 8 * c)); }
; __device__ __forceinline__ void conv_item(Frame& F, const Args& a, int it, LAS float* scr, int lane) {
;     ...
;         if (r < TI_FD) { const int i = r / (44 * 16), q = r % (44 * 16), kt = q / 16, nt = q % 16;
;             tr_item((a.in[22] + F.zo) + (size_t)i * DFF * D, D, 64 * kt, 64 * nt, (bf16*)(ws + WS_FF + i * FF_STRIDE) + (size_t)2 * DFF * D, DFF, 64 * nt, false, scr, lane); break; }
.LBB13_57:
	v_lshl_add_u64 v[52:53], v[20:21], 0, s[28:29]
	v_add_co_u32_e32 v44, vcc, 0x4000, v52
	global_load_dwordx4 v[40:43], v[52:53], off nt
	s_nop 0
	v_addc_co_u32_e32 v45, vcc, 0, v53, vcc
	v_add_co_u32_e32 v48, vcc, 0x8000, v52
	global_load_dwordx4 v[44:47], v[44:45], off nt
	s_nop 0
	v_addc_co_u32_e32 v49, vcc, 0, v53, vcc
	v_add_co_u32_e32 v52, vcc, 0xc000, v52
	global_load_dwordx4 v[48:51], v[48:49], off nt
	s_nop 0
	v_addc_co_u32_e32 v53, vcc, 0, v53, vcc
	global_load_dwordx4 v[52:55], v[52:53], off nt
	s_add_u32 s28, s28, 0x10000
	s_addc_u32 s29, s29, 0
	v_add_u32_e32 v39, 0x410, v4
	v_add_u32_e32 v56, 0x418, v4
	v_add_u32_e32 v57, 0x820, v4
	v_add_u32_e32 v58, 0x828, v4
	v_add_u32_e32 v59, 0xc30, v4
	v_add_u32_e32 v60, 0xc38, v4
	s_cmp_lg_u32 s28, 0x40000
	s_waitcnt vmcnt(3)
	ds_write2_b32 v4, v40, v41 offset1:1
	ds_write2_b32 v4, v42, v43 offset0:2 offset1:3
	v_add_u32_e32 v4, 0x1040, v4
	s_waitcnt vmcnt(2)
	ds_write2_b32 v39, v44, v45 offset1:1
	ds_write2_b32 v56, v46, v47 offset1:1
	s_waitcnt vmcnt(1)
	ds_write2_b32 v57, v48, v49 offset1:1
	ds_write2_b32 v58, v50, v51 offset1:1
	s_waitcnt vmcnt(0)
	ds_write2_b32 v59, v52, v53 offset1:1
	ds_write2_b32 v60, v54, v55 offset1:1
	s_cbranch_scc1 .LBB13_57
	s_lshl_b32 s28, s31, 6
	s_and_b32 s28, s28, 0x3c0
	s_and_b64 s[18:19], s[18:19], exec
	s_cselect_b32 s18, 0x1080000, 0
	s_add_u32 s18, s33, s18
	s_waitcnt lgkmcnt(0)
	v_add_u32_e32 v39, 0x400, v22
	s_addc_u32 s19, s43, 0
	s_lshl_b32 s6, s6, 1
	ds_read2_b32 v[44:45], v22 offset0:65 offset1:73
	ds_read2_b32 v[46:47], v22 offset1:8
	ds_read2_b32 v[48:49], v22 offset0:130 offset1:138
	ds_read2_b32 v[50:51], v22 offset0:195 offset1:203
	ds_read2_b32 v[52:53], v39 offset0:4 offset1:12
	ds_read2_b32 v[54:55], v39 offset0:69 offset1:77
	ds_read2_b32 v[56:57], v39 offset0:134 offset1:142
	ds_read2_b32 v[58:59], v39 offset0:199 offset1:207
	s_add_u32 s18, s18, s6
	s_addc_u32 s19, s19, 0
	v_lshlrev_b32_e32 v4, 1, v2
	v_lshl_add_u64 v[20:21], s[18:19], 0, v[4:5]
	v_or_b32_e32 v4, s28, v1
	v_lshl_add_u64 v[20:21], v[20:21], 0, s[10:11]
	v_mul_u32_u24_e32 v4, 0x1600, v4
	s_waitcnt lgkmcnt(6)
	v_cvt_pk_bf16_f32 v40, v46, v44
	s_waitcnt lgkmcnt(4)
	v_cvt_pk_bf16_f32 v41, v48, v50
	s_waitcnt lgkmcnt(2)
	v_cvt_pk_bf16_f32 v42, v52, v54
	s_waitcnt lgkmcnt(0)
	v_cvt_pk_bf16_f32 v43, v56, v58
	v_lshl_add_u64 v[60:61], v[20:21], 0, v[4:5]
	global_store_dwordx4 v[60:61], v[40:43], off
	v_or_b32_e32 v4, s28, v23
	v_mul_u32_u24_e32 v4, 0x1600, v4
	v_cvt_pk_bf16_f32 v40, v47, v45
	v_cvt_pk_bf16_f32 v41, v49, v51
	v_cvt_pk_bf16_f32 v42, v53, v55
	v_cvt_pk_bf16_f32 v43, v57, v59
	ds_read2_b32 v[46:47], v22 offset0:16 offset1:24
	ds_read2_b32 v[48:49], v22 offset0:81 offset1:89
	ds_read2_b32 v[50:51], v22 offset0:146 offset1:154
	ds_read2_b32 v[52:53], v22 offset0:211 offset1:219
	ds_read2_b32 v[54:55], v39 offset0:20 offset1:28
	ds_read2_b32 v[56:57], v39 offset0:85 offset1:93
	ds_read2_b32 v[58:59], v39 offset0:150 offset1:158
	ds_read2_b32 v[60:61], v39 offset0:215 offset1:223
	v_lshl_add_u64 v[44:45], v[20:21], 0, v[4:5]
	v_or_b32_e32 v4, s28, v24
	v_mul_u32_u24_e32 v4, 0x1600, v4
	global_store_dwordx4 v[44:45], v[40:43], off
	v_lshl_add_u64 v[44:45], v[20:21], 0, v[4:5]
	v_or_b32_e32 v4, s28, v25
	s_waitcnt lgkmcnt(6)
	v_cvt_pk_bf16_f32 v40, v46, v48
	s_waitcnt lgkmcnt(4)
	v_cvt_pk_bf16_f32 v41, v50, v52
	s_waitcnt lgkmcnt(2)
	v_cvt_pk_bf16_f32 v42, v54, v56
	s_waitcnt lgkmcnt(0)
	v_cvt_pk_bf16_f32 v43, v58, v60
	global_store_dwordx4 v[44:45], v[40:43], off
	v_mul_u32_u24_e32 v4, 0x1600, v4
	v_lshl_add_u64 v[44:45], v[20:21], 0, v[4:5]
	v_cvt_pk_bf16_f32 v40, v47, v49
	v_cvt_pk_bf16_f32 v41, v51, v53
	v_cvt_pk_bf16_f32 v42, v55, v57
	v_cvt_pk_bf16_f32 v43, v59, v61
	ds_read2_b32 v[46:47], v22 offset0:32 offset1:40
	ds_read2_b32 v[48:49], v22 offset0:97 offset1:105
	ds_read2_b32 v[50:51], v22 offset0:162 offset1:170
	ds_read2_b32 v[52:53], v22 offset0:227 offset1:235
	ds_read2_b32 v[54:55], v39 offset0:36 offset1:44
	ds_read2_b32 v[56:57], v39 offset0:101 offset1:109
	ds_read2_b32 v[58:59], v39 offset0:166 offset1:174
	ds_read2_b32 v[60:61], v39 offset0:231 offset1:239
	v_or_b32_e32 v4, s28, v26
	v_mul_u32_u24_e32 v4, 0x1600, v4
	global_store_dwordx4 v[44:45], v[40:43], off
	v_lshl_add_u64 v[44:45], v[20:21], 0, v[4:5]
	v_or_b32_e32 v4, s28, v27
	s_waitcnt lgkmcnt(6)
	v_cvt_pk_bf16_f32 v40, v46, v48
	s_waitcnt lgkmcnt(4)
	v_cvt_pk_bf16_f32 v41, v50, v52
	s_waitcnt lgkmcnt(2)
	v_cvt_pk_bf16_f32 v42, v54, v56
	s_waitcnt lgkmcnt(0)
	v_cvt_pk_bf16_f32 v43, v58, v60
	global_store_dwordx4 v[44:45], v[40:43], off
	v_mul_u32_u24_e32 v4, 0x1600, v4
	v_lshl_add_u64 v[44:45], v[20:21], 0, v[4:5]
	v_cvt_pk_bf16_f32 v40, v47, v49
	v_cvt_pk_bf16_f32 v41, v51, v53
	v_cvt_pk_bf16_f32 v42, v55, v57
	v_cvt_pk_bf16_f32 v43, v59, v61
	ds_read2_b32 v[46:47], v22 offset0:48 offset1:56
	ds_read2_b32 v[48:49], v22 offset0:113 offset1:121
	ds_read2_b32 v[50:51], v22 offset0:178 offset1:186
	ds_read2_b32 v[52:53], v22 offset0:243 offset1:251
	ds_read2_b32 v[54:55], v39 offset0:52 offset1:60
	ds_read2_b32 v[56:57], v39 offset0:117 offset1:125
	ds_read2_b32 v[58:59], v39 offset0:182 offset1:190
	ds_read2_b32 v[60:61], v39 offset0:247 offset1:255
	v_or_b32_e32 v4, s28, v28
	v_mul_u32_u24_e32 v4, 0x1600, v4
	global_store_dwordx4 v[44:45], v[40:43], off
	v_lshl_add_u64 v[44:45], v[20:21], 0, v[4:5]
	v_or_b32_e32 v4, s28, v29
	s_waitcnt lgkmcnt(6)
	v_cvt_pk_bf16_f32 v40, v46, v48
	s_waitcnt lgkmcnt(4)
	v_cvt_pk_bf16_f32 v41, v50, v52
	s_waitcnt lgkmcnt(2)
	v_cvt_pk_bf16_f32 v42, v54, v56
	s_waitcnt lgkmcnt(0)
	v_cvt_pk_bf16_f32 v43, v58, v60
	v_mul_u32_u24_e32 v4, 0x1600, v4
	global_store_dwordx4 v[44:45], v[40:43], off
	v_lshl_add_u64 v[20:21], v[20:21], 0, v[4:5]
	s_nop 0
	v_cvt_pk_bf16_f32 v40, v47, v49
	v_cvt_pk_bf16_f32 v41, v51, v53
	v_cvt_pk_bf16_f32 v42, v55, v57
	v_cvt_pk_bf16_f32 v43, v59, v61
	global_store_dwordx4 v[20:21], v[40:43], off
	s_waitcnt lgkmcnt(0)

; #define LAS __attribute__((address_space(3)))
; __device__ __forceinline__ unsigned pk2(float lo, float hi) { f32x2 v = {lo, hi}; return __builtin_bit_cast(unsigned, __builtin_convertvector(v, bf2_t)); }
;     ...
;     for (int i = 0; i < 16; ++i) { const int k = 4 * i + kr; const f32x4 v = __builtin_nontemporal_load((const f32x4*)(s + (size_t)k * ld + 4 * nq));
;         LAS float* d = scr + k * 65 + 4 * nq; d[0] = v[0]; d[1] = v[1]; d[2] = v[2]; d[3] = v[3]; }
;     asm volatile("s_waitcnt lgkmcnt(0)" ::: "memory");
;     const int c = lane & 7;
; #pragma unroll
;     for (int j = 0; j < 8; ++j) { const int n = (lane >> 3) + 8 * j; const int sc_ = qkperm ? ((n & 1) * 32 + (n >> 1)) : n; const LAS float* p = scr + (8 * c) * 65 + sc_;
;         u32x4 o; o.x = pk2(p[0] * scale, p[65] * scale); o.y = pk2(p[130] * scale, p[195] * scale); o.z = pk2(p[260] * scale, p[325] * scale); o.w = pk2(p[390] * scale, p[455] * scale);
;         __builtin_nontemporal_store(o, (u32x4*)(dst + (size_t)(n0 + n) * Kd + k0 + 8 * c)); }
; __device__ __forceinline__ void conv_item(Frame& F, const Args& a, int it, LAS float* scr, int lane) {
;     ...
;         if (r < TI_FGU) { const int i = r / (16 * 88), q = r % (16 * 88), kt = q / 88, nt = q % 88;
;             const int pn = nt >> 2, bj = (nt >> 1) & 1, hf = nt & 1;
;             const float* src = (bj ? (a.in[21] + F.zo) : (a.in[20] + F.zo)) + (size_t)i * D * DFF;
;             tr_item(src, DFF, 64 * kt, 128 * pn + 64 * hf, (bf16*)(ws + WS_FF + i * FF_STRIDE), D, 64 * nt, false, scr, lane); break; }
.LBB13_62:
	v_lshl_add_u64 v[52:53], v[20:21], 0, s[28:29]
	v_add_co_u32_e32 v44, vcc, 0xb000, v52
	global_load_dwordx4 v[40:43], v[52:53], off nt
	s_nop 0
	v_addc_co_u32_e32 v45, vcc, 0, v53, vcc
	v_add_co_u32_e32 v48, vcc, 0x16000, v52
	global_load_dwordx4 v[44:47], v[44:45], off nt
	s_nop 0
	v_addc_co_u32_e32 v49, vcc, 0, v53, vcc
	v_add_co_u32_e32 v52, vcc, 0x21000, v52
	global_load_dwordx4 v[48:51], v[48:49], off nt
	s_nop 0
	v_addc_co_u32_e32 v53, vcc, 0, v53, vcc
	global_load_dwordx4 v[52:55], v[52:53], off nt
	s_add_u32 s28, s28, 0x2c000
	s_addc_u32 s29, s29, 0
	v_add_u32_e32 v39, 0x410, v4
	v_add_u32_e32 v56, 0x418, v4
	v_add_u32_e32 v57, 0x820, v4
	v_add_u32_e32 v58, 0x828, v4
	v_add_u32_e32 v59, 0xc30, v4
	v_add_u32_e32 v60, 0xc38, v4
	s_cmp_lg_u32 s28, 0xb0000
	s_waitcnt vmcnt(3)
	ds_write2_b32 v4, v40, v41 offset1:1
	ds_write2_b32 v4, v42, v43 offset0:2 offset1:3
	v_add_u32_e32 v4, 0x1040, v4
	s_waitcnt vmcnt(2)
	ds_write2_b32 v39, v44, v45 offset1:1
	ds_write2_b32 v56, v46, v47 offset1:1
	s_waitcnt vmcnt(1)
	ds_write2_b32 v57, v48, v49 offset1:1
	ds_write2_b32 v58, v50, v51 offset1:1
	s_waitcnt vmcnt(0)
	ds_write2_b32 v59, v52, v53 offset1:1
	ds_write2_b32 v60, v54, v55 offset1:1
	s_cbranch_scc1 .LBB13_62
	s_and_b64 s[18:19], s[18:19], exec
	s_cselect_b32 s18, 0x1080000, 0
	s_add_u32 s18, s38, s18
	s_waitcnt lgkmcnt(0)
	v_add_u32_e32 v39, 0x400, v22
	s_addc_u32 s19, s39, 0
	s_lshl_b32 s28, s31, 1
	ds_read2_b32 v[20:21], v22 offset0:65 offset1:73
	ds_read2_b32 v[44:45], v22 offset1:8
	ds_read2_b32 v[46:47], v22 offset0:130 offset1:138
	ds_read2_b32 v[48:49], v22 offset0:195 offset1:203
	ds_read2_b32 v[50:51], v39 offset0:4 offset1:12
	ds_read2_b32 v[52:53], v39 offset0:69 offset1:77
	ds_read2_b32 v[54:55], v39 offset0:134 offset1:142
	ds_read2_b32 v[56:57], v39 offset0:199 offset1:207
	s_add_u32 s18, s18, s28
	s_addc_u32 s19, s19, 0
	v_lshlrev_b32_e32 v4, 1, v2
	v_lshl_add_u64 v[58:59], s[18:19], 0, v[4:5]
	v_or_b32_e32 v4, s6, v1
	v_lshlrev_b32_e32 v4, 11, v4
	s_waitcnt lgkmcnt(6)
	v_cvt_pk_bf16_f32 v40, v44, v20
	s_waitcnt lgkmcnt(4)
	v_cvt_pk_bf16_f32 v41, v46, v48
	s_waitcnt lgkmcnt(2)
	v_cvt_pk_bf16_f32 v42, v50, v52
	s_waitcnt lgkmcnt(0)
	v_cvt_pk_bf16_f32 v43, v54, v56
	v_lshl_add_u64 v[60:61], v[58:59], 0, v[4:5]
	global_store_dwordx4 v[60:61], v[40:43], off
	v_or_b32_e32 v4, s6, v23
	v_lshlrev_b32_e32 v4, 11, v4
	v_cvt_pk_bf16_f32 v40, v45, v21
	v_cvt_pk_bf16_f32 v41, v47, v49
	v_cvt_pk_bf16_f32 v42, v51, v53
	v_cvt_pk_bf16_f32 v43, v55, v57
	ds_read2_b32 v[44:45], v22 offset0:81 offset1:89
	ds_read2_b32 v[46:47], v22 offset0:16 offset1:24
	ds_read2_b32 v[48:49], v22 offset0:146 offset1:154
	ds_read2_b32 v[50:51], v22 offset0:211 offset1:219
	ds_read2_b32 v[52:53], v39 offset0:20 offset1:28
	ds_read2_b32 v[54:55], v39 offset0:85 offset1:93
	ds_read2_b32 v[56:57], v39 offset0:150 offset1:158
	ds_read2_b32 v[60:61], v39 offset0:215 offset1:223
	v_lshl_add_u64 v[20:21], v[58:59], 0, v[4:5]
	v_or_b32_e32 v4, s6, v24
	v_lshlrev_b32_e32 v4, 11, v4
	global_store_dwordx4 v[20:21], v[40:43], off
	v_lshl_add_u64 v[20:21], v[58:59], 0, v[4:5]
	v_or_b32_e32 v4, s6, v25
	s_waitcnt lgkmcnt(6)
	v_cvt_pk_bf16_f32 v40, v46, v44
	s_waitcnt lgkmcnt(4)
	v_cvt_pk_bf16_f32 v41, v48, v50
	s_waitcnt lgkmcnt(2)
	v_cvt_pk_bf16_f32 v42, v52, v54
	s_waitcnt lgkmcnt(0)
	v_cvt_pk_bf16_f32 v43, v56, v60
	global_store_dwordx4 v[20:21], v[40:43], off
	v_lshlrev_b32_e32 v4, 11, v4
	v_lshl_add_u64 v[20:21], v[58:59], 0, v[4:5]
	v_cvt_pk_bf16_f32 v40, v47, v45
	v_cvt_pk_bf16_f32 v41, v49, v51
	v_cvt_pk_bf16_f32 v42, v53, v55
	v_cvt_pk_bf16_f32 v43, v57, v61
	ds_read2_b32 v[44:45], v22 offset0:32 offset1:40
	ds_read2_b32 v[46:47], v22 offset0:97 offset1:105
	ds_read2_b32 v[48:49], v22 offset0:162 offset1:170
	ds_read2_b32 v[50:51], v22 offset0:227 offset1:235
	ds_read2_b32 v[52:53], v39 offset0:36 offset1:44
	ds_read2_b32 v[54:55], v39 offset0:101 offset1:109
	ds_read2_b32 v[56:57], v39 offset0:166 offset1:174
	ds_read2_b32 v[60:61], v39 offset0:231 offset1:239
	v_or_b32_e32 v4, s6, v26
	v_lshlrev_b32_e32 v4, 11, v4
	global_store_dwordx4 v[20:21], v[40:43], off
	v_lshl_add_u64 v[20:21], v[58:59], 0, v[4:5]
	v_or_b32_e32 v4, s6, v27
	s_waitcnt lgkmcnt(6)
	v_cvt_pk_bf16_f32 v40, v44, v46
	s_waitcnt lgkmcnt(4)
	v_cvt_pk_bf16_f32 v41, v48, v50
	s_waitcnt lgkmcnt(2)
	v_cvt_pk_bf16_f32 v42, v52, v54
	s_waitcnt lgkmcnt(0)
	v_cvt_pk_bf16_f32 v43, v56, v60
	global_store_dwordx4 v[20:21], v[40:43], off
	v_lshlrev_b32_e32 v4, 11, v4
	v_lshl_add_u64 v[20:21], v[58:59], 0, v[4:5]
	v_cvt_pk_bf16_f32 v40, v45, v47
	v_cvt_pk_bf16_f32 v41, v49, v51
	v_cvt_pk_bf16_f32 v42, v53, v55
	v_cvt_pk_bf16_f32 v43, v57, v61
	ds_read2_b32 v[44:45], v22 offset0:48 offset1:56
	ds_read2_b32 v[46:47], v22 offset0:113 offset1:121
	ds_read2_b32 v[48:49], v22 offset0:178 offset1:186
	ds_read2_b32 v[50:51], v22 offset0:243 offset1:251
	ds_read2_b32 v[52:53], v39 offset0:52 offset1:60
	ds_read2_b32 v[54:55], v39 offset0:117 offset1:125
	ds_read2_b32 v[56:57], v39 offset0:182 offset1:190
	ds_read2_b32 v[60:61], v39 offset0:247 offset1:255
	v_or_b32_e32 v4, s6, v28
	v_lshlrev_b32_e32 v4, 11, v4
	global_store_dwordx4 v[20:21], v[40:43], off
	v_lshl_add_u64 v[20:21], v[58:59], 0, v[4:5]
	v_or_b32_e32 v4, s6, v29
	s_waitcnt lgkmcnt(6)
	v_cvt_pk_bf16_f32 v40, v44, v46
	s_waitcnt lgkmcnt(4)
	v_cvt_pk_bf16_f32 v41, v48, v50
	s_waitcnt lgkmcnt(2)
	v_cvt_pk_bf16_f32 v42, v52, v54
	s_waitcnt lgkmcnt(0)
	v_cvt_pk_bf16_f32 v43, v56, v60
	v_lshlrev_b32_e32 v4, 11, v4
	global_store_dwordx4 v[20:21], v[40:43], off
	v_lshl_add_u64 v[20:21], v[58:59], 0, v[4:5]
	s_nop 0
	v_cvt_pk_bf16_f32 v40, v45, v47
	v_cvt_pk_bf16_f32 v41, v49, v51
	v_cvt_pk_bf16_f32 v42, v53, v55
	v_cvt_pk_bf16_f32 v43, v57, v61
	global_store_dwordx4 v[20:21], v[40:43], off
	s_waitcnt lgkmcnt(0)

; #define LAS __attribute__((address_space(3)))
; __device__ __forceinline__ unsigned pk2(float lo, float hi) { f32x2 v = {lo, hi}; return __builtin_bit_cast(unsigned, __builtin_convertvector(v, bf2_t)); }
;     ...
;     for (int i = 0; i < 16; ++i) { const int k = 4 * i + kr; const f32x4 v = __builtin_nontemporal_load((const f32x4*)(s + (size_t)k * ld + 4 * nq));
;         LAS float* d = scr + k * 65 + 4 * nq; d[0] = v[0]; d[1] = v[1]; d[2] = v[2]; d[3] = v[3]; }
;     asm volatile("s_waitcnt lgkmcnt(0)" ::: "memory");
;     const int c = lane & 7;
; #pragma unroll
;     for (int j = 0; j < 8; ++j) { const int n = (lane >> 3) + 8 * j; const int sc_ = qkperm ? ((n & 1) * 32 + (n >> 1)) : n; const LAS float* p = scr + (8 * c) * 65 + sc_;
;         u32x4 o; o.x = pk2(p[0] * scale, p[65] * scale); o.y = pk2(p[130] * scale, p[195] * scale); o.z = pk2(p[260] * scale, p[325] * scale); o.w = pk2(p[390] * scale, p[455] * scale);
;         __builtin_nontemporal_store(o, (u32x4*)(dst + (size_t)(n0 + n) * Kd + k0 + 8 * c)); }
; __device__ __forceinline__ void conv_item(Frame& F, const Args& a, int it, LAS float* scr, int lane) {
;     ...
;         if (r < TI_WO) { const int mi = r / 256, q = r % 256, kt = q / 16, nt = q % 16, l = mi / 3, w = mi % 3;
;             const float* src = (w == 0 ? (a.in[17] + F.zo) : (w == 1 ? (a.in[18] + F.zo) : (a.in[19] + F.zo))) + (size_t)l * D * D;
;             tr_item(src, D, 64 * kt, 64 * nt, (bf16*)(ws + WS_WO) + (size_t)mi * D * D, D, 64 * nt, false, scr, lane); break; }
.LBB13_67:
	v_lshl_add_u64 v[52:53], v[20:21], 0, s[28:29]
	v_add_co_u32_e32 v44, vcc, 0x4000, v52
	global_load_dwordx4 v[40:43], v[52:53], off nt
	s_nop 0
	v_addc_co_u32_e32 v45, vcc, 0, v53, vcc
	v_add_co_u32_e32 v48, vcc, 0x8000, v52
	global_load_dwordx4 v[44:47], v[44:45], off nt
	s_nop 0
	v_addc_co_u32_e32 v49, vcc, 0, v53, vcc
	v_add_co_u32_e32 v52, vcc, 0xc000, v52
	global_load_dwordx4 v[48:51], v[48:49], off nt
	s_nop 0
	v_addc_co_u32_e32 v53, vcc, 0, v53, vcc
	global_load_dwordx4 v[52:55], v[52:53], off nt
	s_add_u32 s28, s28, 0x10000
	s_addc_u32 s29, s29, 0
	v_add_u32_e32 v39, 0x410, v4
	v_add_u32_e32 v56, 0x418, v4
	v_add_u32_e32 v57, 0x820, v4
	v_add_u32_e32 v58, 0x828, v4
	v_add_u32_e32 v59, 0xc30, v4
	v_add_u32_e32 v60, 0xc38, v4
	s_cmp_lg_u32 s28, 0x40000
	s_waitcnt vmcnt(3)
	ds_write2_b32 v4, v40, v41 offset1:1
	ds_write2_b32 v4, v42, v43 offset0:2 offset1:3
	v_add_u32_e32 v4, 0x1040, v4
	s_waitcnt vmcnt(2)
	ds_write2_b32 v39, v44, v45 offset1:1
	ds_write2_b32 v56, v46, v47 offset1:1
	s_waitcnt vmcnt(1)
	ds_write2_b32 v57, v48, v49 offset1:1
	ds_write2_b32 v58, v50, v51 offset1:1
	s_waitcnt vmcnt(0)
	ds_write2_b32 v59, v52, v53 offset1:1
	ds_write2_b32 v60, v54, v55 offset1:1
	s_cbranch_scc1 .LBB13_67
	s_lshl_b32 s6, s2, 6
	s_mov_b32 s19, s7
	s_and_b32 s6, s6, 0x3c0
	s_lshl_b64 s[18:19], s[18:19], 21
	s_add_u32 s18, s40, s18
	s_addc_u32 s19, s41, s19
	s_waitcnt lgkmcnt(0)
	s_lshl_b32 s28, s2, 3
	v_add_u32_e32 v39, 0x400, v22
	s_and_b32 s28, s28, 0x780
	ds_read2_b32 v[20:21], v22 offset0:65 offset1:73
	ds_read2_b32 v[44:45], v22 offset1:8
	ds_read2_b32 v[46:47], v22 offset0:130 offset1:138
	ds_read2_b32 v[48:49], v22 offset0:195 offset1:203
	ds_read2_b32 v[50:51], v39 offset0:4 offset1:12
	ds_read2_b32 v[52:53], v39 offset0:69 offset1:77
	ds_read2_b32 v[54:55], v39 offset0:134 offset1:142
	ds_read2_b32 v[56:57], v39 offset0:199 offset1:207
	s_add_u32 s18, s18, s28
	s_addc_u32 s19, s19, 0
	v_lshlrev_b32_e32 v4, 1, v2
	v_lshl_add_u64 v[58:59], s[18:19], 0, v[4:5]
	v_or_b32_e32 v4, s6, v1
	v_lshlrev_b32_e32 v4, 11, v4
	s_waitcnt lgkmcnt(6)
	v_cvt_pk_bf16_f32 v40, v44, v20
	s_waitcnt lgkmcnt(4)
	v_cvt_pk_bf16_f32 v41, v46, v48
	s_waitcnt lgkmcnt(2)
	v_cvt_pk_bf16_f32 v42, v50, v52
	s_waitcnt lgkmcnt(0)
	v_cvt_pk_bf16_f32 v43, v54, v56
	v_lshl_add_u64 v[60:61], v[58:59], 0, v[4:5]
	global_store_dwordx4 v[60:61], v[40:43], off
	v_or_b32_e32 v4, s6, v23
	v_lshlrev_b32_e32 v4, 11, v4
	v_cvt_pk_bf16_f32 v40, v45, v21
	v_cvt_pk_bf16_f32 v41, v47, v49
	v_cvt_pk_bf16_f32 v42, v51, v53
	v_cvt_pk_bf16_f32 v43, v55, v57
	ds_read2_b32 v[44:45], v22 offset0:81 offset1:89
	ds_read2_b32 v[46:47], v22 offset0:16 offset1:24
	ds_read2_b32 v[48:49], v22 offset0:146 offset1:154
	ds_read2_b32 v[50:51], v22 offset0:211 offset1:219
	ds_read2_b32 v[52:53], v39 offset0:20 offset1:28
	ds_read2_b32 v[54:55], v39 offset0:85 offset1:93
	ds_read2_b32 v[56:57], v39 offset0:150 offset1:158
	ds_read2_b32 v[60:61], v39 offset0:215 offset1:223
	v_lshl_add_u64 v[20:21], v[58:59], 0, v[4:5]
	v_or_b32_e32 v4, s6, v24
	v_lshlrev_b32_e32 v4, 11, v4
	global_store_dwordx4 v[20:21], v[40:43], off
	v_lshl_add_u64 v[20:21], v[58:59], 0, v[4:5]
	v_or_b32_e32 v4, s6, v25
	s_waitcnt lgkmcnt(6)
	v_cvt_pk_bf16_f32 v40, v46, v44
	s_waitcnt lgkmcnt(4)
	v_cvt_pk_bf16_f32 v41, v48, v50
	s_waitcnt lgkmcnt(2)
	v_cvt_pk_bf16_f32 v42, v52, v54
	s_waitcnt lgkmcnt(0)
	v_cvt_pk_bf16_f32 v43, v56, v60
	global_store_dwordx4 v[20:21], v[40:43], off
	v_lshlrev_b32_e32 v4, 11, v4
	v_lshl_add_u64 v[20:21], v[58:59], 0, v[4:5]
	v_cvt_pk_bf16_f32 v40, v47, v45
	v_cvt_pk_bf16_f32 v41, v49, v51
	v_cvt_pk_bf16_f32 v42, v53, v55
	v_cvt_pk_bf16_f32 v43, v57, v61
	ds_read2_b32 v[44:45], v22 offset0:32 offset1:40
	ds_read2_b32 v[46:47], v22 offset0:97 offset1:105
	ds_read2_b32 v[48:49], v22 offset0:162 offset1:170
	ds_read2_b32 v[50:51], v22 offset0:227 offset1:235
	ds_read2_b32 v[52:53], v39 offset0:36 offset1:44
	ds_read2_b32 v[54:55], v39 offset0:101 offset1:109
	ds_read2_b32 v[56:57], v39 offset0:166 offset1:174
	ds_read2_b32 v[60:61], v39 offset0:231 offset1:239
	v_or_b32_e32 v4, s6, v26
	v_lshlrev_b32_e32 v4, 11, v4
	global_store_dwordx4 v[20:21], v[40:43], off
	v_lshl_add_u64 v[20:21], v[58:59], 0, v[4:5]
	v_or_b32_e32 v4, s6, v27
	s_waitcnt lgkmcnt(6)
	v_cvt_pk_bf16_f32 v40, v44, v46
	s_waitcnt lgkmcnt(4)
	v_cvt_pk_bf16_f32 v41, v48, v50
	s_waitcnt lgkmcnt(2)
	v_cvt_pk_bf16_f32 v42, v52, v54
	s_waitcnt lgkmcnt(0)
	v_cvt_pk_bf16_f32 v43, v56, v60
	global_store_dwordx4 v[20:21], v[40:43], off
	v_lshlrev_b32_e32 v4, 11, v4
	v_lshl_add_u64 v[20:21], v[58:59], 0, v[4:5]
	v_cvt_pk_bf16_f32 v40, v45, v47
	v_cvt_pk_bf16_f32 v41, v49, v51
	v_cvt_pk_bf16_f32 v42, v53, v55
	v_cvt_pk_bf16_f32 v43, v57, v61
	ds_read2_b32 v[44:45], v22 offset0:48 offset1:56
	ds_read2_b32 v[46:47], v22 offset0:113 offset1:121
	ds_read2_b32 v[48:49], v22 offset0:178 offset1:186
	ds_read2_b32 v[50:51], v22 offset0:243 offset1:251
	ds_read2_b32 v[52:53], v39 offset0:52 offset1:60
	ds_read2_b32 v[54:55], v39 offset0:117 offset1:125
	ds_read2_b32 v[56:57], v39 offset0:182 offset1:190
	ds_read2_b32 v[60:61], v39 offset0:247 offset1:255
	v_or_b32_e32 v4, s6, v28
	v_lshlrev_b32_e32 v4, 11, v4
	global_store_dwordx4 v[20:21], v[40:43], off
	v_lshl_add_u64 v[20:21], v[58:59], 0, v[4:5]
	v_or_b32_e32 v4, s6, v29
	s_waitcnt lgkmcnt(6)
	v_cvt_pk_bf16_f32 v40, v44, v46
	s_waitcnt lgkmcnt(4)
	v_cvt_pk_bf16_f32 v41, v48, v50
	s_waitcnt lgkmcnt(2)
	v_cvt_pk_bf16_f32 v42, v52, v54
	s_waitcnt lgkmcnt(0)
	v_cvt_pk_bf16_f32 v43, v56, v60
	v_lshlrev_b32_e32 v4, 11, v4
	global_store_dwordx4 v[20:21], v[40:43], off
	v_lshl_add_u64 v[20:21], v[58:59], 0, v[4:5]
	s_nop 0
	v_cvt_pk_bf16_f32 v40, v45, v47
	v_cvt_pk_bf16_f32 v41, v49, v51
	v_cvt_pk_bf16_f32 v42, v53, v55
	v_cvt_pk_bf16_f32 v43, v57, v61
	global_store_dwordx4 v[20:21], v[40:43], off
	s_waitcnt lgkmcnt(0)

; #define LAS __attribute__((address_space(3)))
; __device__ __forceinline__ unsigned pk2(float lo, float hi) { f32x2 v = {lo, hi}; return __builtin_bit_cast(unsigned, __builtin_convertvector(v, bf2_t)); }
;     ...
;     for (int i = 0; i < 16; ++i) { const int k = 4 * i + kr; const f32x4 v = __builtin_nontemporal_load((const f32x4*)(s + (size_t)k * ld + 4 * nq));
;         LAS float* d = scr + k * 65 + 4 * nq; d[0] = v[0]; d[1] = v[1]; d[2] = v[2]; d[3] = v[3]; }
;     asm volatile("s_waitcnt lgkmcnt(0)" ::: "memory");
;     const int c = lane & 7;
; #pragma unroll
;     for (int j = 0; j < 8; ++j) { const int n = (lane >> 3) + 8 * j; const int sc_ = qkperm ? ((n & 1) * 32 + (n >> 1)) : n; const LAS float* p = scr + (8 * c) * 65 + sc_;
;         u32x4 o; o.x = pk2(p[0] * scale, p[65] * scale); o.y = pk2(p[130] * scale, p[195] * scale); o.z = pk2(p[260] * scale, p[325] * scale); o.w = pk2(p[390] * scale, p[455] * scale);
;         __builtin_nontemporal_store(o, (u32x4*)(dst + (size_t)(n0 + n) * Kd + k0 + 8 * c)); }
; __device__ __forceinline__ void conv_item(Frame& F, const Args& a, int it, LAS float* scr, int lane) {
;     ...
;         if (r < TI_GT) { const int tl = r & 3, m = r >> 2, h = m & 7, gx = (m >> 3) & 1, d = (m >> 4) & 1, l = m >> 5;
;             const float* src = (gx ? (a.in[14] + F.zo) : (a.in[12] + F.zo)) + (size_t)((l * 2 + d) * 8 + h) * 128 * 128;
;             bf16* dst = (bf16*)(ws + WS_GT) + (size_t)((l * 8 + h) * 4 + 2 * d + gx) * 128 * 128;
;             tr_item(src, 128, 64 * (tl >> 1), 64 * (tl & 1), dst, 128, 64 * (tl & 1), false, scr, lane, -1.4426950408889634f); break; }
.LBB13_72:
	v_lshl_add_u64 v[48:49], v[20:21], 0, s[18:19]
	v_add_co_u32_e32 v52, vcc, s51, v48
	global_load_dwordx4 v[40:43], v[48:49], off nt
	global_load_dwordx4 v[44:47], v[48:49], off offset:2048 nt
	v_addc_co_u32_e32 v53, vcc, 0, v49, vcc
	global_load_dwordx4 v[48:51], v[52:53], off nt
	s_nop 0
	global_load_dwordx4 v[52:55], v[52:53], off offset:2048 nt
	s_add_u32 s18, s18, 0x2000
	s_addc_u32 s19, s19, 0
	v_add_u32_e32 v39, 0x410, v4
	v_add_u32_e32 v56, 0x418, v4
	v_add_u32_e32 v57, 0x820, v4
	v_add_u32_e32 v58, 0x828, v4
	v_add_u32_e32 v59, 0xc30, v4
	v_add_u32_e32 v60, 0xc38, v4
	s_cmpk_lg_u32 s18, 0x8000
	s_waitcnt vmcnt(3)
	ds_write2_b32 v4, v40, v41 offset1:1
	ds_write2_b32 v4, v42, v43 offset0:2 offset1:3
	s_waitcnt vmcnt(2)
	ds_write2_b32 v39, v44, v45 offset1:1
	ds_write2_b32 v56, v46, v47 offset1:1
	v_add_u32_e32 v4, 0x1040, v4
	s_waitcnt vmcnt(1)
	ds_write2_b32 v57, v48, v49 offset1:1
	ds_write2_b32 v58, v50, v51 offset1:1
	s_waitcnt vmcnt(0)
	ds_write2_b32 v59, v52, v53 offset1:1
	ds_write2_b32 v60, v54, v55 offset1:1
	s_cbranch_scc1 .LBB13_72
	s_add_i32 s18, s2, 0xffffea00
	s_lshr_b32 s18, s18, 2
	s_and_b32 s18, s18, 0x3fffffe0
	s_and_b32 s19, s2, 28
	s_or_b32 s18, s18, s19
	s_lshr_b32 s19, s2, 5
	s_and_b32 s19, s19, 2
	s_waitcnt lgkmcnt(0)
	s_or_b32 s18, s18, s19
	ds_read2_b32 v[44:45], v22 offset1:8
	ds_read2_b32 v[46:47], v22 offset0:65 offset1:73
	ds_read2_b32 v[48:49], v22 offset0:130 offset1:138
	ds_read2_b32 v[50:51], v22 offset0:195 offset1:203
	s_or_b32 s6, s18, s6
	s_lshl_b32 s19, s2, 6
	v_add_u32_e32 v39, 0x400, v22
	s_and_b32 s18, s19, 64
	s_lshl_b64 s[28:29], s[6:7], 15
	ds_read2_b32 v[52:53], v39 offset0:4 offset1:12
	ds_read2_b32 v[54:55], v39 offset0:69 offset1:77
	ds_read2_b32 v[56:57], v39 offset0:134 offset1:142
	ds_read2_b32 v[58:59], v39 offset0:199 offset1:207
	s_add_u32 s6, s42, s28
	s_addc_u32 s29, s44, s29
	s_and_b32 s19, s19, 0x80
	s_add_u32 s28, s6, s19
	s_waitcnt lgkmcnt(7)
	v_mov_b32_e32 v40, v44
	s_waitcnt lgkmcnt(6)
	v_mov_b32_e32 v41, v46
	s_waitcnt lgkmcnt(5)
	v_mov_b32_e32 v42, v48
	s_waitcnt lgkmcnt(4)
	v_mov_b32_e32 v43, v50
	s_addc_u32 s29, s29, 0
	v_lshlrev_b32_e32 v4, 1, v2
	v_pk_mul_f32 v[40:41], v[40:41], s[14:15] op_sel_hi:[1,0]
	v_pk_mul_f32 v[42:43], v[42:43], s[14:15] op_sel_hi:[1,0]
	v_lshl_add_u64 v[20:21], s[28:29], 0, v[4:5]
	v_cvt_pk_bf16_f32 v40, v40, v41
	v_cvt_pk_bf16_f32 v41, v42, v43
	s_waitcnt lgkmcnt(3)
	v_mov_b32_e32 v42, v52
	s_waitcnt lgkmcnt(2)
	v_mov_b32_e32 v43, v54
	s_waitcnt lgkmcnt(1)
	v_mov_b32_e32 v60, v56
	s_waitcnt lgkmcnt(0)
	v_mov_b32_e32 v61, v58
	v_or_b32_e32 v4, s18, v1
	v_pk_mul_f32 v[42:43], v[42:43], s[14:15] op_sel_hi:[1,0]
	v_pk_mul_f32 v[60:61], v[60:61], s[14:15] op_sel_hi:[1,0]
	v_lshlrev_b32_e32 v4, 8, v4
	v_cvt_pk_bf16_f32 v42, v42, v43
	v_cvt_pk_bf16_f32 v43, v60, v61
	v_lshl_add_u64 v[60:61], v[20:21], 0, v[4:5]
	v_mov_b32_e32 v46, v45
	v_mov_b32_e32 v50, v49
	global_store_dwordx4 v[60:61], v[40:43], off
	v_mov_b32_e32 v54, v53
	v_mov_b32_e32 v58, v57
	v_pk_mul_f32 v[40:41], v[46:47], s[14:15] op_sel_hi:[1,0]
	v_pk_mul_f32 v[42:43], v[50:51], s[14:15] op_sel_hi:[1,0]
	v_or_b32_e32 v4, s18, v23
	v_cvt_pk_bf16_f32 v40, v40, v41
	v_cvt_pk_bf16_f32 v41, v42, v43
	v_pk_mul_f32 v[42:43], v[54:55], s[14:15] op_sel_hi:[1,0]
	v_pk_mul_f32 v[44:45], v[58:59], s[14:15] op_sel_hi:[1,0]
	v_lshlrev_b32_e32 v4, 8, v4
	v_cvt_pk_bf16_f32 v42, v42, v43
	v_cvt_pk_bf16_f32 v43, v44, v45
	v_lshl_add_u64 v[48:49], v[20:21], 0, v[4:5]
	ds_read2_b32 v[44:45], v22 offset0:16 offset1:24
	ds_read2_b32 v[46:47], v22 offset0:81 offset1:89
	global_store_dwordx4 v[48:49], v[40:43], off
	ds_read2_b32 v[48:49], v22 offset0:146 offset1:154
	ds_read2_b32 v[50:51], v22 offset0:211 offset1:219
	ds_read2_b32 v[52:53], v39 offset0:20 offset1:28
	ds_read2_b32 v[54:55], v39 offset0:85 offset1:93
	ds_read2_b32 v[56:57], v39 offset0:150 offset1:158
	ds_read2_b32 v[58:59], v39 offset0:215 offset1:223
	s_waitcnt lgkmcnt(7)
	v_mov_b32_e32 v40, v44
	s_waitcnt lgkmcnt(6)
	v_mov_b32_e32 v41, v46
	s_waitcnt lgkmcnt(5)
	v_mov_b32_e32 v42, v48
	s_waitcnt lgkmcnt(4)
	v_mov_b32_e32 v43, v50
	v_pk_mul_f32 v[40:41], v[40:41], s[14:15] op_sel_hi:[1,0]
	v_pk_mul_f32 v[42:43], v[42:43], s[14:15] op_sel_hi:[1,0]
	v_cvt_pk_bf16_f32 v40, v40, v41
	v_cvt_pk_bf16_f32 v41, v42, v43
	s_waitcnt lgkmcnt(3)
	v_mov_b32_e32 v42, v52
	s_waitcnt lgkmcnt(2)
	v_mov_b32_e32 v43, v54
	s_waitcnt lgkmcnt(1)
	v_mov_b32_e32 v60, v56
	s_waitcnt lgkmcnt(0)
; #define LAS __attribute__((address_space(3)))
; __device__ __forceinline__ unsigned pk2(float lo, float hi) { f32x2 v = {lo, hi}; return __builtin_bit_cast(unsigned, __builtin_convertvector(v, bf2_t)); }
;     ...
;     for (int j = 0; j < 8; ++j) { const int n = (lane >> 3) + 8 * j; const int sc_ = qkperm ? ((n & 1) * 32 + (n >> 1)) : n; const LAS float* p = scr + (8 * c) * 65 + sc_;
;         u32x4 o; o.x = pk2(p[0] * scale, p[65] * scale); o.y = pk2(p[130] * scale, p[195] * scale); o.z = pk2(p[260] * scale, p[325] * scale); o.w = pk2(p[390] * scale, p[455] * scale);
;         __builtin_nontemporal_store(o, (u32x4*)(dst + (size_t)(n0 + n) * Kd + k0 + 8 * c)); }
	v_mov_b32_e32 v61, v58
	v_or_b32_e32 v4, s18, v24
	v_pk_mul_f32 v[42:43], v[42:43], s[14:15] op_sel_hi:[1,0]
	v_pk_mul_f32 v[60:61], v[60:61], s[14:15] op_sel_hi:[1,0]
	v_lshlrev_b32_e32 v4, 8, v4
	v_cvt_pk_bf16_f32 v42, v42, v43
	v_cvt_pk_bf16_f32 v43, v60, v61
	v_lshl_add_u64 v[60:61], v[20:21], 0, v[4:5]
	v_mov_b32_e32 v46, v45
	v_mov_b32_e32 v50, v49
	global_store_dwordx4 v[60:61], v[40:43], off
	v_mov_b32_e32 v54, v53
	v_mov_b32_e32 v58, v57
	v_pk_mul_f32 v[40:41], v[46:47], s[14:15] op_sel_hi:[1,0]
	v_pk_mul_f32 v[42:43], v[50:51], s[14:15] op_sel_hi:[1,0]
	v_or_b32_e32 v4, s18, v25
	v_cvt_pk_bf16_f32 v40, v40, v41
	v_cvt_pk_bf16_f32 v41, v42, v43
	v_pk_mul_f32 v[42:43], v[54:55], s[14:15] op_sel_hi:[1,0]
	v_pk_mul_f32 v[44:45], v[58:59], s[14:15] op_sel_hi:[1,0]
	v_lshlrev_b32_e32 v4, 8, v4
	v_cvt_pk_bf16_f32 v42, v42, v43
	v_cvt_pk_bf16_f32 v43, v44, v45
	v_lshl_add_u64 v[48:49], v[20:21], 0, v[4:5]
	ds_read2_b32 v[44:45], v22 offset0:32 offset1:40
	ds_read2_b32 v[46:47], v22 offset0:97 offset1:105
	global_store_dwordx4 v[48:49], v[40:43], off
	ds_read2_b32 v[48:49], v22 offset0:162 offset1:170
	ds_read2_b32 v[50:51], v22 offset0:227 offset1:235
	ds_read2_b32 v[52:53], v39 offset0:36 offset1:44
	ds_read2_b32 v[54:55], v39 offset0:101 offset1:109
	ds_read2_b32 v[56:57], v39 offset0:166 offset1:174
	ds_read2_b32 v[58:59], v39 offset0:231 offset1:239
	s_waitcnt lgkmcnt(7)
	v_mov_b32_e32 v40, v44
	s_waitcnt lgkmcnt(6)
	v_mov_b32_e32 v41, v46
	s_waitcnt lgkmcnt(5)
	v_mov_b32_e32 v42, v48
	s_waitcnt lgkmcnt(4)
	v_mov_b32_e32 v43, v50
	v_pk_mul_f32 v[40:41], v[40:41], s[14:15] op_sel_hi:[1,0]
	v_pk_mul_f32 v[42:43], v[42:43], s[14:15] op_sel_hi:[1,0]
	v_cvt_pk_bf16_f32 v40, v40, v41
	v_cvt_pk_bf16_f32 v41, v42, v43
	s_waitcnt lgkmcnt(3)
	v_mov_b32_e32 v42, v52
	s_waitcnt lgkmcnt(2)
	v_mov_b32_e32 v43, v54
	s_waitcnt lgkmcnt(1)
	v_mov_b32_e32 v60, v56
	s_waitcnt lgkmcnt(0)
	v_mov_b32_e32 v61, v58
	v_or_b32_e32 v4, s18, v26
	v_pk_mul_f32 v[42:43], v[42:43], s[14:15] op_sel_hi:[1,0]
	v_pk_mul_f32 v[60:61], v[60:61], s[14:15] op_sel_hi:[1,0]
	v_lshlrev_b32_e32 v4, 8, v4
	v_cvt_pk_bf16_f32 v42, v42, v43
	v_cvt_pk_bf16_f32 v43, v60, v61
	v_lshl_add_u64 v[60:61], v[20:21], 0, v[4:5]
	v_mov_b32_e32 v46, v45
	v_mov_b32_e32 v50, v49
	global_store_dwordx4 v[60:61], v[40:43], off
	v_mov_b32_e32 v54, v53
	v_mov_b32_e32 v58, v57
	v_pk_mul_f32 v[40:41], v[46:47], s[14:15] op_sel_hi:[1,0]
	v_pk_mul_f32 v[42:43], v[50:51], s[14:15] op_sel_hi:[1,0]
	v_or_b32_e32 v4, s18, v27
	v_cvt_pk_bf16_f32 v40, v40, v41
	v_cvt_pk_bf16_f32 v41, v42, v43
	v_pk_mul_f32 v[42:43], v[54:55], s[14:15] op_sel_hi:[1,0]
	v_pk_mul_f32 v[44:45], v[58:59], s[14:15] op_sel_hi:[1,0]
	v_lshlrev_b32_e32 v4, 8, v4
	v_cvt_pk_bf16_f32 v42, v42, v43
	v_cvt_pk_bf16_f32 v43, v44, v45
	v_lshl_add_u64 v[48:49], v[20:21], 0, v[4:5]
	ds_read2_b32 v[44:45], v22 offset0:48 offset1:56
	ds_read2_b32 v[46:47], v22 offset0:113 offset1:121
	global_store_dwordx4 v[48:49], v[40:43], off
	ds_read2_b32 v[48:49], v22 offset0:178 offset1:186
	ds_read2_b32 v[50:51], v22 offset0:243 offset1:251
	ds_read2_b32 v[52:53], v39 offset0:52 offset1:60
	ds_read2_b32 v[54:55], v39 offset0:117 offset1:125
	ds_read2_b32 v[56:57], v39 offset0:182 offset1:190
	ds_read2_b32 v[58:59], v39 offset0:247 offset1:255
	s_waitcnt lgkmcnt(7)
	v_mov_b32_e32 v40, v44
	s_waitcnt lgkmcnt(6)
	v_mov_b32_e32 v41, v46
	s_waitcnt lgkmcnt(5)
	v_mov_b32_e32 v42, v48
	s_waitcnt lgkmcnt(4)
	v_mov_b32_e32 v43, v50
	v_pk_mul_f32 v[40:41], v[40:41], s[14:15] op_sel_hi:[1,0]
	v_pk_mul_f32 v[42:43], v[42:43], s[14:15] op_sel_hi:[1,0]
	v_cvt_pk_bf16_f32 v40, v40, v41
	v_cvt_pk_bf16_f32 v41, v42, v43
	s_waitcnt lgkmcnt(3)
	v_mov_b32_e32 v42, v52
	s_waitcnt lgkmcnt(2)
	v_mov_b32_e32 v43, v54
	s_waitcnt lgkmcnt(1)
	v_mov_b32_e32 v60, v56
	s_waitcnt lgkmcnt(0)
	v_mov_b32_e32 v61, v58
	v_or_b32_e32 v4, s18, v28
	v_pk_mul_f32 v[42:43], v[42:43], s[14:15] op_sel_hi:[1,0]
	v_pk_mul_f32 v[60:61], v[60:61], s[14:15] op_sel_hi:[1,0]
	v_lshlrev_b32_e32 v4, 8, v4
	v_cvt_pk_bf16_f32 v42, v42, v43
	v_cvt_pk_bf16_f32 v43, v60, v61
	v_lshl_add_u64 v[60:61], v[20:21], 0, v[4:5]
	v_mov_b32_e32 v46, v45
	v_mov_b32_e32 v50, v49
	global_store_dwordx4 v[60:61], v[40:43], off
	v_mov_b32_e32 v54, v53
	v_mov_b32_e32 v58, v57
	v_pk_mul_f32 v[40:41], v[46:47], s[14:15] op_sel_hi:[1,0]
	v_pk_mul_f32 v[42:43], v[50:51], s[14:15] op_sel_hi:[1,0]
	v_or_b32_e32 v4, s18, v29
	v_cvt_pk_bf16_f32 v40, v40, v41
	v_cvt_pk_bf16_f32 v41, v42, v43
	v_pk_mul_f32 v[42:43], v[54:55], s[14:15] op_sel_hi:[1,0]
	v_pk_mul_f32 v[44:45], v[58:59], s[14:15] op_sel_hi:[1,0]
	v_lshlrev_b32_e32 v4, 8, v4
	v_cvt_pk_bf16_f32 v42, v42, v43
	v_cvt_pk_bf16_f32 v43, v44, v45
	v_lshl_add_u64 v[20:21], v[20:21], 0, v[4:5]
	global_store_dwordx4 v[20:21], v[40:43], off
	s_waitcnt lgkmcnt(0)

; #define LAS __attribute__((address_space(3)))
;     ...
;     for (int i = 0; i < 16; ++i) { const int k = 4 * i + kr; const f32x4 v = __builtin_nontemporal_load((const f32x4*)(s + (size_t)k * ld + 4 * nq));
;         LAS float* d = scr + k * 65 + 4 * nq; d[0] = v[0]; d[1] = v[1]; d[2] = v[2]; d[3] = v[3]; }
.LBB13_77:
	v_lshl_add_u64 v[52:53], v[20:21], 0, s[30:31]
	v_add_co_u32_e32 v44, vcc, 0x16000, v52
	global_load_dwordx4 v[40:43], v[52:53], off nt
	s_nop 0
	v_addc_co_u32_e32 v45, vcc, 0, v53, vcc
	v_add_co_u32_e32 v48, vcc, 0x2c000, v52
	global_load_dwordx4 v[44:47], v[44:45], off nt
	s_nop 0
	v_addc_co_u32_e32 v49, vcc, 0, v53, vcc
	v_add_co_u32_e32 v52, vcc, 0x42000, v52
	global_load_dwordx4 v[48:51], v[48:49], off nt
	s_nop 0
	v_addc_co_u32_e32 v53, vcc, 0, v53, vcc
	global_load_dwordx4 v[52:55], v[52:53], off nt
	s_add_u32 s30, s30, 0x58000
	s_addc_u32 s31, s31, 0
	v_add_u32_e32 v39, 0x410, v4
	v_add_u32_e32 v56, 0x418, v4
	v_add_u32_e32 v57, 0x820, v4
	v_add_u32_e32 v58, 0x828, v4
	v_add_u32_e32 v59, 0xc30, v4
	v_add_u32_e32 v60, 0xc38, v4
	s_cmp_lg_u32 s30, 0x160000
	s_waitcnt vmcnt(3)
	ds_write2_b32 v4, v40, v41 offset1:1
	ds_write2_b32 v4, v42, v43 offset0:2 offset1:3
	v_add_u32_e32 v4, 0x1040, v4
	s_waitcnt vmcnt(2)
	ds_write2_b32 v39, v44, v45 offset1:1
	ds_write2_b32 v56, v46, v47 offset1:1
	s_waitcnt vmcnt(1)
	ds_write2_b32 v57, v48, v49 offset1:1
	ds_write2_b32 v58, v50, v51 offset1:1
	s_waitcnt vmcnt(0)
	ds_write2_b32 v59, v52, v53 offset1:1
	ds_write2_b32 v60, v54, v55 offset1:1
	s_cbranch_scc1 .LBB13_77
; #define LAS __attribute__((address_space(3)))
; __device__ __forceinline__ unsigned pk2(float lo, float hi) { f32x2 v = {lo, hi}; return __builtin_bit_cast(unsigned, __builtin_convertvector(v, bf2_t)); }
;     ...
;     for (int j = 0; j < 8; ++j) { const int n = (lane >> 3) + 8 * j; const int sc_ = qkperm ? ((n & 1) * 32 + (n >> 1)) : n; const LAS float* p = scr + (8 * c) * 65 + sc_;
;         u32x4 o; o.x = pk2(p[0] * scale, p[65] * scale); o.y = pk2(p[130] * scale, p[195] * scale); o.z = pk2(p[260] * scale, p[325] * scale); o.w = pk2(p[390] * scale, p[455] * scale);
;         __builtin_nontemporal_store(o, (u32x4*)(dst + (size_t)(n0 + n) * Kd + k0 + 8 * c)); }
; __device__ __forceinline__ void conv_item(Frame& F, const Args& a, int it, LAS float* scr, int lane) {
;     ...
;         if (r < TI_WIN) { const int l = r / (16 * 88), q = r % (16 * 88), kt = q / 88, nt = q % 88;
;             tr_item((a.in[8] + F.zo) + (size_t)l * D * INC, INC, 64 * kt, 64 * nt, (bf16*)(ws + WS_WIN) + (size_t)l * INC * D, D, 64 * nt, nt < 20, scr, lane); break; }
	s_mul_hi_i32 s19, s6, 0xb00000
	s_mul_i32 s6, s6, 0xb00000
	s_add_u32 s6, s45, s6
	s_addc_u32 s19, s46, s19
	s_cmp_lt_i32 s52, 20
	s_cselect_b64 vcc, -1, 0
	v_cndmask_b32_e32 v20, v1, v30, vcc
	s_waitcnt lgkmcnt(0)
	v_lshl_add_u32 v39, v20, 2, v3
	ds_read2_b32 v[20:21], v39 offset1:65
	ds_read2_b32 v[42:43], v39 offset0:130 offset1:195
	v_add_u32_e32 v39, 0x400, v39
	s_lshl_b64 s[28:29], s[28:29], 1
	ds_read2_b32 v[44:45], v39 offset0:4 offset1:69
	ds_read2_b32 v[46:47], v39 offset0:134 offset1:199
	s_add_u32 s28, s6, s28
	s_addc_u32 s29, s19, s29
	v_lshlrev_b32_e32 v4, 1, v2
	v_lshl_add_u64 v[48:49], s[28:29], 0, v[4:5]
	v_cndmask_b32_e32 v4, v23, v31, vcc
	v_lshl_add_u32 v4, v4, 2, v3
	s_waitcnt lgkmcnt(3)
	v_cvt_pk_bf16_f32 v40, v20, v21
	s_waitcnt lgkmcnt(2)
	v_cvt_pk_bf16_f32 v41, v42, v43
	s_waitcnt lgkmcnt(1)
	v_cvt_pk_bf16_f32 v42, v44, v45
	s_waitcnt lgkmcnt(0)
	v_cvt_pk_bf16_f32 v43, v46, v47
	v_or_b32_e32 v20, s18, v1
	ds_read2_b32 v[44:45], v4 offset1:65
	ds_read2_b32 v[46:47], v4 offset0:130 offset1:195
	v_add_u32_e32 v4, 0x400, v4
	v_ashrrev_i32_e32 v21, 31, v20
	ds_read2_b32 v[50:51], v4 offset0:4 offset1:69
	ds_read2_b32 v[52:53], v4 offset0:134 offset1:199
	v_lshlrev_b64 v[20:21], 11, v[20:21]
	v_lshl_add_u64 v[20:21], v[48:49], 0, v[20:21]
	v_cndmask_b32_e32 v4, v24, v32, vcc
	global_store_dwordx4 v[20:21], v[40:43], off
	v_lshl_add_u32 v4, v4, 2, v3
	v_or_b32_e32 v20, s18, v23
	s_waitcnt lgkmcnt(3)
	v_cvt_pk_bf16_f32 v40, v44, v45
	s_waitcnt lgkmcnt(2)
	v_cvt_pk_bf16_f32 v41, v46, v47
	ds_read2_b32 v[44:45], v4 offset1:65
	ds_read2_b32 v[46:47], v4 offset0:130 offset1:195
	v_add_u32_e32 v4, 0x400, v4
	s_waitcnt lgkmcnt(3)
	v_cvt_pk_bf16_f32 v42, v50, v51
	s_waitcnt lgkmcnt(2)
	v_cvt_pk_bf16_f32 v43, v52, v53
	v_ashrrev_i32_e32 v21, 31, v20
	ds_read2_b32 v[50:51], v4 offset0:4 offset1:69
	ds_read2_b32 v[52:53], v4 offset0:134 offset1:199
	v_lshlrev_b64 v[20:21], 11, v[20:21]
	v_lshl_add_u64 v[20:21], v[48:49], 0, v[20:21]
	v_cndmask_b32_e32 v4, v25, v33, vcc
	global_store_dwordx4 v[20:21], v[40:43], off
	v_lshl_add_u32 v4, v4, 2, v3
	v_or_b32_e32 v20, s18, v24
	s_waitcnt lgkmcnt(3)
	v_cvt_pk_bf16_f32 v40, v44, v45
	s_waitcnt lgkmcnt(2)
	v_cvt_pk_bf16_f32 v41, v46, v47
	ds_read2_b32 v[44:45], v4 offset1:65
	ds_read2_b32 v[46:47], v4 offset0:130 offset1:195
	v_add_u32_e32 v4, 0x400, v4
	s_waitcnt lgkmcnt(3)
	v_cvt_pk_bf16_f32 v42, v50, v51
	s_waitcnt lgkmcnt(2)
	v_cvt_pk_bf16_f32 v43, v52, v53
	v_ashrrev_i32_e32 v21, 31, v20
	ds_read2_b32 v[50:51], v4 offset0:4 offset1:69
	ds_read2_b32 v[52:53], v4 offset0:134 offset1:199
	v_lshlrev_b64 v[20:21], 11, v[20:21]
	v_lshl_add_u64 v[20:21], v[48:49], 0, v[20:21]
	v_cndmask_b32_e32 v4, v26, v34, vcc
	global_store_dwordx4 v[20:21], v[40:43], off
	v_lshl_add_u32 v4, v4, 2, v3
	v_or_b32_e32 v20, s18, v25
	s_waitcnt lgkmcnt(3)
	v_cvt_pk_bf16_f32 v40, v44, v45
	s_waitcnt lgkmcnt(2)
	v_cvt_pk_bf16_f32 v41, v46, v47
	ds_read2_b32 v[44:45], v4 offset1:65
	ds_read2_b32 v[46:47], v4 offset0:130 offset1:195
	v_add_u32_e32 v4, 0x400, v4
	s_waitcnt lgkmcnt(3)
	v_cvt_pk_bf16_f32 v42, v50, v51
	s_waitcnt lgkmcnt(2)
	v_cvt_pk_bf16_f32 v43, v52, v53
	v_ashrrev_i32_e32 v21, 31, v20
	ds_read2_b32 v[50:51], v4 offset0:4 offset1:69
	ds_read2_b32 v[52:53], v4 offset0:134 offset1:199
	v_lshlrev_b64 v[20:21], 11, v[20:21]
	v_lshl_add_u64 v[20:21], v[48:49], 0, v[20:21]
	v_cndmask_b32_e32 v4, v27, v35, vcc
	global_store_dwordx4 v[20:21], v[40:43], off
	v_lshl_add_u32 v4, v4, 2, v3
	v_or_b32_e32 v20, s18, v26
	s_waitcnt lgkmcnt(3)
	v_cvt_pk_bf16_f32 v40, v44, v45
	s_waitcnt lgkmcnt(2)
	v_cvt_pk_bf16_f32 v41, v46, v47
	ds_read2_b32 v[44:45], v4 offset1:65
	ds_read2_b32 v[46:47], v4 offset0:130 offset1:195
	v_add_u32_e32 v4, 0x400, v4
	s_waitcnt lgkmcnt(3)
	v_cvt_pk_bf16_f32 v42, v50, v51
	s_waitcnt lgkmcnt(2)
	v_cvt_pk_bf16_f32 v43, v52, v53
	v_ashrrev_i32_e32 v21, 31, v20
	ds_read2_b32 v[50:51], v4 offset0:4 offset1:69
	ds_read2_b32 v[52:53], v4 offset0:134 offset1:199
	v_lshlrev_b64 v[20:21], 11, v[20:21]
	v_lshl_add_u64 v[20:21], v[48:49], 0, v[20:21]
	v_cndmask_b32_e32 v4, v28, v36, vcc
	global_store_dwordx4 v[20:21], v[40:43], off
	v_lshl_add_u32 v4, v4, 2, v3
	v_or_b32_e32 v20, s18, v27
	s_waitcnt lgkmcnt(3)
	v_cvt_pk_bf16_f32 v40, v44, v45
	s_waitcnt lgkmcnt(2)
	v_cvt_pk_bf16_f32 v41, v46, v47
	ds_read2_b32 v[44:45], v4 offset1:65
	ds_read2_b32 v[46:47], v4 offset0:130 offset1:195
	v_add_u32_e32 v4, 0x400, v4
	s_waitcnt lgkmcnt(3)
	v_cvt_pk_bf16_f32 v42, v50, v51
	s_waitcnt lgkmcnt(2)
	v_cvt_pk_bf16_f32 v43, v52, v53
	v_ashrrev_i32_e32 v21, 31, v20
	ds_read2_b32 v[50:51], v4 offset0:4 offset1:69
	ds_read2_b32 v[52:53], v4 offset0:134 offset1:199
	v_lshlrev_b64 v[20:21], 11, v[20:21]
	v_lshl_add_u64 v[20:21], v[48:49], 0, v[20:21]
	v_cndmask_b32_e32 v4, v29, v37, vcc
	global_store_dwordx4 v[20:21], v[40:43], off
	v_or_b32_e32 v20, s18, v28
	v_lshl_add_u32 v4, v4, 2, v3
	s_waitcnt lgkmcnt(3)
	v_cvt_pk_bf16_f32 v40, v44, v45
	s_waitcnt lgkmcnt(2)
	v_cvt_pk_bf16_f32 v41, v46, v47
	v_ashrrev_i32_e32 v21, 31, v20
	ds_read2_b32 v[44:45], v4 offset1:65
	ds_read2_b32 v[46:47], v4 offset0:130 offset1:195
	v_add_u32_e32 v4, 0x400, v4
	s_waitcnt lgkmcnt(3)
	v_cvt_pk_bf16_f32 v42, v50, v51
	s_waitcnt lgkmcnt(2)
	v_cvt_pk_bf16_f32 v43, v52, v53
	v_lshlrev_b64 v[20:21], 11, v[20:21]
	ds_read2_b32 v[50:51], v4 offset0:4 offset1:69
	ds_read2_b32 v[52:53], v4 offset0:134 offset1:199
	v_lshl_add_u64 v[20:21], v[48:49], 0, v[20:21]
	global_store_dwordx4 v[20:21], v[40:43], off
	v_or_b32_e32 v20, s18, v29
	v_ashrrev_i32_e32 v21, 31, v20
	v_lshlrev_b64 v[20:21], 11, v[20:21]
	s_waitcnt lgkmcnt(3)
	v_cvt_pk_bf16_f32 v40, v44, v45
	s_waitcnt lgkmcnt(2)
	v_cvt_pk_bf16_f32 v41, v46, v47
	s_waitcnt lgkmcnt(1)
	v_cvt_pk_bf16_f32 v42, v50, v51
	s_waitcnt lgkmcnt(0)
	v_cvt_pk_bf16_f32 v43, v52, v53
	v_lshl_add_u64 v[20:21], v[48:49], 0, v[20:21]
	global_store_dwordx4 v[20:21], v[40:43], off
	s_waitcnt lgkmcnt(0)
	s_branch .LBB13_40
